# router: logit loop fully unrolled (no register rotate), router weight staging with all loads issued up front
# speedup vs baseline: 1.0062x; 1.0062x over previous
; #define LAS __attribute__((address_space(3)))
; DI KArgP kargs() { KArgP p = (KArgP)__builtin_amdgcn_kernarg_segment_ptr(); asm volatile("" : "+s"(p)); return p; }
; template <int l>
; DI void layer_body(LAS unsigned char* lds, const XcdBarrier& bar, const int lo, const int hi, const int G, const int vcu) {
;     ...
;             else { const float* wr = kargs()->in[13] + (size_t)(l / 2) * D_ * NE; LAS float* wT = (LAS float*)lds;
;                 for (int c = tid; c < D_; c += 512) { const f32x4 a = *(const f32x4*)(wr + (size_t)c * 8), b = *(const f32x4*)(wr + (size_t)c * 8 + 4);
;                     LAS float* wp = wT + ((c >> 2) & 1) * 1024 + ((c >> 9) * 64 + ((c >> 3) & 63)) * 4 + (c & 3);
;                     wp[0] = a[0]; wp[2048] = a[1]; wp[2 * 2048] = a[2]; wp[3 * 2048] = a[3]; wp[4 * 2048] = b[0]; wp[5 * 2048] = b[1]; wp[6 * 2048] = b[2]; wp[7 * 2048] = b[3]; }
.LBB0_1369:
	global_load_dwordx4 v[16:19], v[2:3], off offset:-16
	global_load_dwordx4 v[20:23], v[2:3], off
	v_lshl_add_u64 v[6:7], v[2:3], 0, s[16:17]
	global_load_dwordx4 v[24:27], v[6:7], off offset:-16
	global_load_dwordx4 v[28:31], v[6:7], off
	v_lshl_add_u64 v[6:7], v[6:7], 0, s[16:17]
	global_load_dwordx4 v[32:35], v[6:7], off offset:-16
	global_load_dwordx4 v[36:39], v[6:7], off
	v_lshl_add_u64 v[6:7], v[6:7], 0, s[16:17]
	global_load_dwordx4 v[40:43], v[6:7], off offset:-16
	global_load_dwordx4 v[44:47], v[6:7], off
	v_and_b32_e32 v8, 0x400, v4
	v_lshlrev_b32_e32 v15, 1, v5
	v_lshl_add_u32 v8, v8, 2, 0
	v_and_b32_e32 v15, -16, v15
	v_add_u32_e32 v4, 0x20000, v4
	v_add_u32_e32 v5, 0x200, v5
	v_add3_u32 v8, v8, v15, v1
	s_waitcnt vmcnt(7)
	ds_write2st64_b32 v8, v16, v17 offset1:32
	ds_write2st64_b32 v8, v18, v19 offset0:64 offset1:96
	s_waitcnt vmcnt(6)
	ds_write2st64_b32 v8, v20, v21 offset0:128 offset1:160
	ds_write2st64_b32 v8, v22, v23 offset0:192 offset1:224
	v_and_b32_e32 v9, 0x400, v4
	v_lshlrev_b32_e32 v15, 1, v5
	v_lshl_add_u32 v9, v9, 2, 0
	v_and_b32_e32 v15, -16, v15
	v_add_u32_e32 v4, 0x20000, v4
	v_add_u32_e32 v5, 0x200, v5
	v_add3_u32 v9, v9, v15, v1
	s_waitcnt vmcnt(5)
	ds_write2st64_b32 v9, v24, v25 offset1:32
	ds_write2st64_b32 v9, v26, v27 offset0:64 offset1:96
	s_waitcnt vmcnt(4)
	ds_write2st64_b32 v9, v28, v29 offset0:128 offset1:160
	ds_write2st64_b32 v9, v30, v31 offset0:192 offset1:224
	v_and_b32_e32 v10, 0x400, v4
	v_lshlrev_b32_e32 v15, 1, v5
	v_lshl_add_u32 v10, v10, 2, 0
	v_and_b32_e32 v15, -16, v15
	v_add_u32_e32 v4, 0x20000, v4
	v_add_u32_e32 v5, 0x200, v5
	v_add3_u32 v10, v10, v15, v1
	s_waitcnt vmcnt(3)
	ds_write2st64_b32 v10, v32, v33 offset1:32
	ds_write2st64_b32 v10, v34, v35 offset0:64 offset1:96
	s_waitcnt vmcnt(2)
	ds_write2st64_b32 v10, v36, v37 offset0:128 offset1:160
	ds_write2st64_b32 v10, v38, v39 offset0:192 offset1:224
	v_and_b32_e32 v11, 0x400, v4
	v_lshlrev_b32_e32 v15, 1, v5
	v_lshl_add_u32 v11, v11, 2, 0
	v_and_b32_e32 v15, -16, v15
	v_add_u32_e32 v4, 0x20000, v4
	v_add_u32_e32 v5, 0x200, v5
	v_add3_u32 v11, v11, v15, v1
	s_waitcnt vmcnt(1)
	ds_write2st64_b32 v11, v40, v41 offset1:32
	ds_write2st64_b32 v11, v42, v43 offset0:64 offset1:96
	s_waitcnt vmcnt(0)
	ds_write2st64_b32 v11, v44, v45 offset0:128 offset1:160
	ds_write2st64_b32 v11, v46, v47 offset0:192 offset1:224

; #define LAS __attribute__((address_space(3)))
; template <bool ROUTE, bool COMBINE> ...
;     ...
;         for (int j = 0; j < 8; ++j) {
;             const f32x4 o = v[0]; const LAS float* wp = wT + (j & 1) * 1024 + ((j >> 1) * 64 + lane) * 4;
;             const f32x4 w0 = *(const LAS f32x4*)(wp), w1 = *(const LAS f32x4*)(wp + 2048), w2 = *(const LAS f32x4*)(wp + 2 * 2048), w3 = *(const LAS f32x4*)(wp + 3 * 2048);
;             const f32x4 w4 = *(const LAS f32x4*)(wp + 4 * 2048), w5 = *(const LAS f32x4*)(wp + 5 * 2048), w6 = *(const LAS f32x4*)(wp + 6 * 2048), w7 = *(const LAS f32x4*)(wp + 7 * 2048);
;             lg0 += (o[0] * w0[0] + o[1] * w0[1]) + (o[2] * w0[2] + o[3] * w0[3]); lg1 += (o[0] * w1[0] + o[1] * w1[1]) + (o[2] * w1[2] + o[3] * w1[3]);
;             lg2 += (o[0] * w2[0] + o[1] * w2[1]) + (o[2] * w2[2] + o[3] * w2[3]); lg3 += (o[0] * w3[0] + o[1] * w3[1]) + (o[2] * w3[2] + o[3] * w3[3]);
;             lg4 += (o[0] * w4[0] + o[1] * w4[1]) + (o[2] * w4[2] + o[3] * w4[3]); lg5 += (o[0] * w5[0] + o[1] * w5[1]) + (o[2] * w5[2] + o[3] * w5[3]);
;             lg6 += (o[0] * w6[0] + o[1] * w6[1]) + (o[2] * w6[2] + o[3] * w6[3]); lg7 += (o[0] * w7[0] + o[1] * w7[1]) + (o[2] * w7[2] + o[3] * w7[3]);
; #pragma unroll
;             for (int jj = 0; jj < 7; ++jj) v[jj] = v[jj + 1];
;         }
.LBB0_1378:
	s_and_b32 s8, s7, 0x400
	s_and_b32 s9, s6, 0xc0
	s_lshl_b32 s8, s8, 2
	v_or_b32_e32 v126, s9, v128
	s_add_i32 s8, s8, 0
	v_lshl_add_u32 v126, v126, 4, s8
	ds_read_b128 v[138:141], v126
	ds_read_b128 v[142:145], v126 offset:8192
	ds_read_b128 v[146:149], v126 offset:16384
	ds_read_b128 v[150:153], v126 offset:24576
	ds_read_b128 v[154:157], v126 offset:32768
	ds_read_b128 v[158:161], v126 offset:40960
	ds_read_b128 v[162:165], v126 offset:49152
	ds_read_b128 v[166:169], v126 offset:57344
	s_waitcnt lgkmcnt(6)
	v_mov_b32_e32 v126, v142
	v_mov_b32_e32 v127, v139
	v_pk_mov_b32 v[138:139], v[142:143], v[138:139] op_sel:[1,0]
	v_mov_b32_e32 v142, v144
	v_mov_b32_e32 v143, v141
	v_pk_mov_b32 v[140:141], v[144:145], v[140:141] op_sel:[1,0]
	s_waitcnt lgkmcnt(4)
	v_pk_mov_b32 v[144:145], v[146:147], v[150:151] op_sel:[1,0]
	v_mov_b32_e32 v147, v151
	v_pk_mov_b32 v[150:151], v[148:149], v[152:153] op_sel:[1,0]
	v_mov_b32_e32 v149, v153
	s_waitcnt lgkmcnt(2)
	v_pk_mov_b32 v[152:153], v[154:155], v[158:159] op_sel:[1,0]
	v_mov_b32_e32 v155, v159
	v_pk_mov_b32 v[158:159], v[156:157], v[160:161] op_sel:[1,0]
	v_mov_b32_e32 v157, v161
	s_waitcnt lgkmcnt(0)
	v_pk_mov_b32 v[160:161], v[162:163], v[166:167] op_sel:[1,0]
	v_mov_b32_e32 v163, v167
	v_pk_mov_b32 v[166:167], v[164:165], v[168:169] op_sel:[1,0]
	v_mov_b32_e32 v165, v169
	v_pk_mul_f32 v[126:127], v[84:85], v[126:127]
	v_pk_mul_f32 v[142:143], v[82:83], v[142:143]
	v_pk_mul_f32 v[146:147], v[84:85], v[146:147]
	v_pk_mul_f32 v[148:149], v[82:83], v[148:149]
	v_pk_mul_f32 v[154:155], v[84:85], v[154:155]
	v_pk_mul_f32 v[156:157], v[82:83], v[156:157]
	v_pk_mul_f32 v[162:163], v[84:85], v[162:163]
	v_pk_mul_f32 v[164:165], v[82:83], v[164:165]
	v_pk_fma_f32 v[126:127], v[84:85], v[138:139], v[126:127] op_sel:[1,0,0] op_sel_hi:[0,1,1]
	v_pk_fma_f32 v[138:139], v[82:83], v[140:141], v[142:143] op_sel:[1,0,0] op_sel_hi:[0,1,1]
	v_pk_fma_f32 v[140:141], v[84:85], v[144:145], v[146:147] op_sel:[1,0,0] op_sel_hi:[0,1,1]
	v_pk_fma_f32 v[142:143], v[82:83], v[150:151], v[148:149] op_sel:[1,0,0] op_sel_hi:[0,1,1]
	v_pk_fma_f32 v[144:145], v[84:85], v[152:153], v[154:155] op_sel:[1,0,0] op_sel_hi:[0,1,1]
	v_pk_fma_f32 v[146:147], v[82:83], v[158:159], v[156:157] op_sel:[1,0,0] op_sel_hi:[0,1,1]
	v_pk_fma_f32 v[148:149], v[84:85], v[160:161], v[162:163] op_sel:[1,0,0] op_sel_hi:[0,1,1]
	v_pk_fma_f32 v[150:151], v[82:83], v[166:167], v[164:165] op_sel:[1,0,0] op_sel_hi:[0,1,1]
	s_addk_i32 s7, 0x400
	s_add_i32 s6, s6, 32
	v_pk_add_f32 v[126:127], v[126:127], v[138:139]
	v_pk_add_f32 v[138:139], v[140:141], v[142:143]
	v_pk_add_f32 v[140:141], v[144:145], v[146:147]
	v_pk_add_f32 v[142:143], v[148:149], v[150:151]
	v_pk_add_f32 v[80:81], v[80:81], v[126:127]
	v_pk_add_f32 v[124:125], v[124:125], v[138:139]
	v_pk_add_f32 v[94:95], v[94:95], v[140:141]
	v_pk_add_f32 v[92:93], v[92:93], v[142:143]
	s_and_b32 s8, s7, 0x400
	s_and_b32 s9, s6, 0xc0
	s_lshl_b32 s8, s8, 2
	v_or_b32_e32 v126, s9, v128
	s_add_i32 s8, s8, 0
	v_lshl_add_u32 v126, v126, 4, s8
	ds_read_b128 v[138:141], v126
	ds_read_b128 v[142:145], v126 offset:8192
	ds_read_b128 v[146:149], v126 offset:16384
	ds_read_b128 v[150:153], v126 offset:24576
	ds_read_b128 v[154:157], v126 offset:32768
	ds_read_b128 v[158:161], v126 offset:40960
	ds_read_b128 v[162:165], v126 offset:49152
	ds_read_b128 v[166:169], v126 offset:57344
	s_waitcnt lgkmcnt(6)
	v_mov_b32_e32 v126, v142
	v_mov_b32_e32 v127, v139
	v_pk_mov_b32 v[138:139], v[142:143], v[138:139] op_sel:[1,0]
	v_mov_b32_e32 v142, v144
	v_mov_b32_e32 v143, v141
	v_pk_mov_b32 v[140:141], v[144:145], v[140:141] op_sel:[1,0]
	s_waitcnt lgkmcnt(4)
	v_pk_mov_b32 v[144:145], v[146:147], v[150:151] op_sel:[1,0]
	v_mov_b32_e32 v147, v151
	v_pk_mov_b32 v[150:151], v[148:149], v[152:153] op_sel:[1,0]
	v_mov_b32_e32 v149, v153
	s_waitcnt lgkmcnt(2)
	v_pk_mov_b32 v[152:153], v[154:155], v[158:159] op_sel:[1,0]
	v_mov_b32_e32 v155, v159
	v_pk_mov_b32 v[158:159], v[156:157], v[160:161] op_sel:[1,0]
	v_mov_b32_e32 v157, v161
	s_waitcnt lgkmcnt(0)
	v_pk_mov_b32 v[160:161], v[162:163], v[166:167] op_sel:[1,0]
	v_mov_b32_e32 v163, v167
	v_pk_mov_b32 v[166:167], v[164:165], v[168:169] op_sel:[1,0]
	v_mov_b32_e32 v165, v169
	v_pk_mul_f32 v[126:127], v[88:89], v[126:127]
	v_pk_mul_f32 v[142:143], v[86:87], v[142:143]
	v_pk_mul_f32 v[146:147], v[88:89], v[146:147]
	v_pk_mul_f32 v[148:149], v[86:87], v[148:149]
	v_pk_mul_f32 v[154:155], v[88:89], v[154:155]
	v_pk_mul_f32 v[156:157], v[86:87], v[156:157]
	v_pk_mul_f32 v[162:163], v[88:89], v[162:163]
	v_pk_mul_f32 v[164:165], v[86:87], v[164:165]
	v_pk_fma_f32 v[126:127], v[88:89], v[138:139], v[126:127] op_sel:[1,0,0] op_sel_hi:[0,1,1]
	v_pk_fma_f32 v[138:139], v[86:87], v[140:141], v[142:143] op_sel:[1,0,0] op_sel_hi:[0,1,1]
	v_pk_fma_f32 v[140:141], v[88:89], v[144:145], v[146:147] op_sel:[1,0,0] op_sel_hi:[0,1,1]
	v_pk_fma_f32 v[142:143], v[86:87], v[150:151], v[148:149] op_sel:[1,0,0] op_sel_hi:[0,1,1]
	v_pk_fma_f32 v[144:145], v[88:89], v[152:153], v[154:155] op_sel:[1,0,0] op_sel_hi:[0,1,1]
	v_pk_fma_f32 v[146:147], v[86:87], v[158:159], v[156:157] op_sel:[1,0,0] op_sel_hi:[0,1,1]
	v_pk_fma_f32 v[148:149], v[88:89], v[160:161], v[162:163] op_sel:[1,0,0] op_sel_hi:[0,1,1]
	v_pk_fma_f32 v[150:151], v[86:87], v[166:167], v[164:165] op_sel:[1,0,0] op_sel_hi:[0,1,1]
	s_addk_i32 s7, 0x400
	s_add_i32 s6, s6, 32
	v_pk_add_f32 v[126:127], v[126:127], v[138:139]
	v_pk_add_f32 v[138:139], v[140:141], v[142:143]
	v_pk_add_f32 v[140:141], v[144:145], v[146:147]
	v_pk_add_f32 v[142:143], v[148:149], v[150:151]
	v_pk_add_f32 v[80:81], v[80:81], v[126:127]
	v_pk_add_f32 v[124:125], v[124:125], v[138:139]
	v_pk_add_f32 v[94:95], v[94:95], v[140:141]
	v_pk_add_f32 v[92:93], v[92:93], v[142:143]
	s_and_b32 s8, s7, 0x400
	s_and_b32 s9, s6, 0xc0
	s_lshl_b32 s8, s8, 2
	v_or_b32_e32 v126, s9, v128
	s_add_i32 s8, s8, 0
	v_lshl_add_u32 v126, v126, 4, s8
	ds_read_b128 v[138:141], v126
	ds_read_b128 v[142:145], v126 offset:8192
	ds_read_b128 v[146:149], v126 offset:16384
	ds_read_b128 v[150:153], v126 offset:24576
	ds_read_b128 v[154:157], v126 offset:32768
	ds_read_b128 v[158:161], v126 offset:40960
	ds_read_b128 v[162:165], v126 offset:49152
	ds_read_b128 v[166:169], v126 offset:57344
	s_waitcnt lgkmcnt(6)
; #define LAS __attribute__((address_space(3)))
; template <bool ROUTE, bool COMBINE> ...
;     ...
;         for (int j = 0; j < 8; ++j) {
;             const f32x4 o = v[0]; const LAS float* wp = wT + (j & 1) * 1024 + ((j >> 1) * 64 + lane) * 4;
;             const f32x4 w0 = *(const LAS f32x4*)(wp), w1 = *(const LAS f32x4*)(wp + 2048), w2 = *(const LAS f32x4*)(wp + 2 * 2048), w3 = *(const LAS f32x4*)(wp + 3 * 2048);
;             const f32x4 w4 = *(const LAS f32x4*)(wp + 4 * 2048), w5 = *(const LAS f32x4*)(wp + 5 * 2048), w6 = *(const LAS f32x4*)(wp + 6 * 2048), w7 = *(const LAS f32x4*)(wp + 7 * 2048);
;             lg0 += (o[0] * w0[0] + o[1] * w0[1]) + (o[2] * w0[2] + o[3] * w0[3]); lg1 += (o[0] * w1[0] + o[1] * w1[1]) + (o[2] * w1[2] + o[3] * w1[3]);
;             lg2 += (o[0] * w2[0] + o[1] * w2[1]) + (o[2] * w2[2] + o[3] * w2[3]); lg3 += (o[0] * w3[0] + o[1] * w3[1]) + (o[2] * w3[2] + o[3] * w3[3]);
;             lg4 += (o[0] * w4[0] + o[1] * w4[1]) + (o[2] * w4[2] + o[3] * w4[3]); lg5 += (o[0] * w5[0] + o[1] * w5[1]) + (o[2] * w5[2] + o[3] * w5[3]);
;             lg6 += (o[0] * w6[0] + o[1] * w6[1]) + (o[2] * w6[2] + o[3] * w6[3]); lg7 += (o[0] * w7[0] + o[1] * w7[1]) + (o[2] * w7[2] + o[3] * w7[3]);
; #pragma unroll
;             for (int jj = 0; jj < 7; ++jj) v[jj] = v[jj + 1];
;         }
	v_mov_b32_e32 v126, v142
	v_mov_b32_e32 v127, v139
	v_pk_mov_b32 v[138:139], v[142:143], v[138:139] op_sel:[1,0]
	v_mov_b32_e32 v142, v144
	v_mov_b32_e32 v143, v141
	v_pk_mov_b32 v[140:141], v[144:145], v[140:141] op_sel:[1,0]
	s_waitcnt lgkmcnt(4)
	v_pk_mov_b32 v[144:145], v[146:147], v[150:151] op_sel:[1,0]
	v_mov_b32_e32 v147, v151
	v_pk_mov_b32 v[150:151], v[148:149], v[152:153] op_sel:[1,0]
	v_mov_b32_e32 v149, v153
	s_waitcnt lgkmcnt(2)
	v_pk_mov_b32 v[152:153], v[154:155], v[158:159] op_sel:[1,0]
	v_mov_b32_e32 v155, v159
	v_pk_mov_b32 v[158:159], v[156:157], v[160:161] op_sel:[1,0]
	v_mov_b32_e32 v157, v161
	s_waitcnt lgkmcnt(0)
	v_pk_mov_b32 v[160:161], v[162:163], v[166:167] op_sel:[1,0]
	v_mov_b32_e32 v163, v167
	v_pk_mov_b32 v[166:167], v[164:165], v[168:169] op_sel:[1,0]
	v_mov_b32_e32 v165, v169
	v_pk_mul_f32 v[126:127], v[110:111], v[126:127]
	v_pk_mul_f32 v[142:143], v[90:91], v[142:143]
	v_pk_mul_f32 v[146:147], v[110:111], v[146:147]
	v_pk_mul_f32 v[148:149], v[90:91], v[148:149]
	v_pk_mul_f32 v[154:155], v[110:111], v[154:155]
	v_pk_mul_f32 v[156:157], v[90:91], v[156:157]
	v_pk_mul_f32 v[162:163], v[110:111], v[162:163]
	v_pk_mul_f32 v[164:165], v[90:91], v[164:165]
	v_pk_fma_f32 v[126:127], v[110:111], v[138:139], v[126:127] op_sel:[1,0,0] op_sel_hi:[0,1,1]
	v_pk_fma_f32 v[138:139], v[90:91], v[140:141], v[142:143] op_sel:[1,0,0] op_sel_hi:[0,1,1]
	v_pk_fma_f32 v[140:141], v[110:111], v[144:145], v[146:147] op_sel:[1,0,0] op_sel_hi:[0,1,1]
	v_pk_fma_f32 v[142:143], v[90:91], v[150:151], v[148:149] op_sel:[1,0,0] op_sel_hi:[0,1,1]
	v_pk_fma_f32 v[144:145], v[110:111], v[152:153], v[154:155] op_sel:[1,0,0] op_sel_hi:[0,1,1]
	v_pk_fma_f32 v[146:147], v[90:91], v[158:159], v[156:157] op_sel:[1,0,0] op_sel_hi:[0,1,1]
	v_pk_fma_f32 v[148:149], v[110:111], v[160:161], v[162:163] op_sel:[1,0,0] op_sel_hi:[0,1,1]
	v_pk_fma_f32 v[150:151], v[90:91], v[166:167], v[164:165] op_sel:[1,0,0] op_sel_hi:[0,1,1]
	s_addk_i32 s7, 0x400
	s_add_i32 s6, s6, 32
	v_pk_add_f32 v[126:127], v[126:127], v[138:139]
	v_pk_add_f32 v[138:139], v[140:141], v[142:143]
	v_pk_add_f32 v[140:141], v[144:145], v[146:147]
	v_pk_add_f32 v[142:143], v[148:149], v[150:151]
	v_pk_add_f32 v[80:81], v[80:81], v[126:127]
	v_pk_add_f32 v[124:125], v[124:125], v[138:139]
	v_pk_add_f32 v[94:95], v[94:95], v[140:141]
	v_pk_add_f32 v[92:93], v[92:93], v[142:143]
	s_and_b32 s8, s7, 0x400
	s_and_b32 s9, s6, 0xc0
	s_lshl_b32 s8, s8, 2
	v_or_b32_e32 v126, s9, v128
	s_add_i32 s8, s8, 0
	v_lshl_add_u32 v126, v126, 4, s8
	ds_read_b128 v[138:141], v126
	ds_read_b128 v[142:145], v126 offset:8192
	ds_read_b128 v[146:149], v126 offset:16384
	ds_read_b128 v[150:153], v126 offset:24576
	ds_read_b128 v[154:157], v126 offset:32768
	ds_read_b128 v[158:161], v126 offset:40960
	ds_read_b128 v[162:165], v126 offset:49152
	ds_read_b128 v[166:169], v126 offset:57344
	s_waitcnt lgkmcnt(6)
	v_mov_b32_e32 v126, v142
	v_mov_b32_e32 v127, v139
	v_pk_mov_b32 v[138:139], v[142:143], v[138:139] op_sel:[1,0]
	v_mov_b32_e32 v142, v144
	v_mov_b32_e32 v143, v141
	v_pk_mov_b32 v[140:141], v[144:145], v[140:141] op_sel:[1,0]
	s_waitcnt lgkmcnt(4)
	v_pk_mov_b32 v[144:145], v[146:147], v[150:151] op_sel:[1,0]
	v_mov_b32_e32 v147, v151
	v_pk_mov_b32 v[150:151], v[148:149], v[152:153] op_sel:[1,0]
	v_mov_b32_e32 v149, v153
	s_waitcnt lgkmcnt(2)
	v_pk_mov_b32 v[152:153], v[154:155], v[158:159] op_sel:[1,0]
	v_mov_b32_e32 v155, v159
	v_pk_mov_b32 v[158:159], v[156:157], v[160:161] op_sel:[1,0]
	v_mov_b32_e32 v157, v161
	s_waitcnt lgkmcnt(0)
	v_pk_mov_b32 v[160:161], v[162:163], v[166:167] op_sel:[1,0]
	v_mov_b32_e32 v163, v167
	v_pk_mov_b32 v[166:167], v[164:165], v[168:169] op_sel:[1,0]
	v_mov_b32_e32 v165, v169
	v_pk_mul_f32 v[126:127], v[114:115], v[126:127]
	v_pk_mul_f32 v[142:143], v[112:113], v[142:143]
	v_pk_mul_f32 v[146:147], v[114:115], v[146:147]
	v_pk_mul_f32 v[148:149], v[112:113], v[148:149]
	v_pk_mul_f32 v[154:155], v[114:115], v[154:155]
	v_pk_mul_f32 v[156:157], v[112:113], v[156:157]
	v_pk_mul_f32 v[162:163], v[114:115], v[162:163]
	v_pk_mul_f32 v[164:165], v[112:113], v[164:165]
	v_pk_fma_f32 v[126:127], v[114:115], v[138:139], v[126:127] op_sel:[1,0,0] op_sel_hi:[0,1,1]
	v_pk_fma_f32 v[138:139], v[112:113], v[140:141], v[142:143] op_sel:[1,0,0] op_sel_hi:[0,1,1]
	v_pk_fma_f32 v[140:141], v[114:115], v[144:145], v[146:147] op_sel:[1,0,0] op_sel_hi:[0,1,1]
	v_pk_fma_f32 v[142:143], v[112:113], v[150:151], v[148:149] op_sel:[1,0,0] op_sel_hi:[0,1,1]
	v_pk_fma_f32 v[144:145], v[114:115], v[152:153], v[154:155] op_sel:[1,0,0] op_sel_hi:[0,1,1]
	v_pk_fma_f32 v[146:147], v[112:113], v[158:159], v[156:157] op_sel:[1,0,0] op_sel_hi:[0,1,1]
	v_pk_fma_f32 v[148:149], v[114:115], v[160:161], v[162:163] op_sel:[1,0,0] op_sel_hi:[0,1,1]
	v_pk_fma_f32 v[150:151], v[112:113], v[166:167], v[164:165] op_sel:[1,0,0] op_sel_hi:[0,1,1]
	s_addk_i32 s7, 0x400
	s_add_i32 s6, s6, 32
	v_pk_add_f32 v[126:127], v[126:127], v[138:139]
	v_pk_add_f32 v[138:139], v[140:141], v[142:143]
	v_pk_add_f32 v[140:141], v[144:145], v[146:147]
	v_pk_add_f32 v[142:143], v[148:149], v[150:151]
	v_pk_add_f32 v[80:81], v[80:81], v[126:127]
	v_pk_add_f32 v[124:125], v[124:125], v[138:139]
	v_pk_add_f32 v[94:95], v[94:95], v[140:141]
	v_pk_add_f32 v[92:93], v[92:93], v[142:143]
	s_and_b32 s8, s7, 0x400
	s_and_b32 s9, s6, 0xc0
	s_lshl_b32 s8, s8, 2
	v_or_b32_e32 v126, s9, v128
	s_add_i32 s8, s8, 0
	v_lshl_add_u32 v126, v126, 4, s8
	ds_read_b128 v[138:141], v126
	ds_read_b128 v[142:145], v126 offset:8192
	ds_read_b128 v[146:149], v126 offset:16384
	ds_read_b128 v[150:153], v126 offset:24576
	ds_read_b128 v[154:157], v126 offset:32768
	ds_read_b128 v[158:161], v126 offset:40960
	ds_read_b128 v[162:165], v126 offset:49152
	ds_read_b128 v[166:169], v126 offset:57344
	s_waitcnt lgkmcnt(6)
; #define LAS __attribute__((address_space(3)))
; template <bool ROUTE, bool COMBINE> ...
;     ...
;         for (int j = 0; j < 8; ++j) {
;             const f32x4 o = v[0]; const LAS float* wp = wT + (j & 1) * 1024 + ((j >> 1) * 64 + lane) * 4;
;             const f32x4 w0 = *(const LAS f32x4*)(wp), w1 = *(const LAS f32x4*)(wp + 2048), w2 = *(const LAS f32x4*)(wp + 2 * 2048), w3 = *(const LAS f32x4*)(wp + 3 * 2048);
;             const f32x4 w4 = *(const LAS f32x4*)(wp + 4 * 2048), w5 = *(const LAS f32x4*)(wp + 5 * 2048), w6 = *(const LAS f32x4*)(wp + 6 * 2048), w7 = *(const LAS f32x4*)(wp + 7 * 2048);
;             lg0 += (o[0] * w0[0] + o[1] * w0[1]) + (o[2] * w0[2] + o[3] * w0[3]); lg1 += (o[0] * w1[0] + o[1] * w1[1]) + (o[2] * w1[2] + o[3] * w1[3]);
;             lg2 += (o[0] * w2[0] + o[1] * w2[1]) + (o[2] * w2[2] + o[3] * w2[3]); lg3 += (o[0] * w3[0] + o[1] * w3[1]) + (o[2] * w3[2] + o[3] * w3[3]);
;             lg4 += (o[0] * w4[0] + o[1] * w4[1]) + (o[2] * w4[2] + o[3] * w4[3]); lg5 += (o[0] * w5[0] + o[1] * w5[1]) + (o[2] * w5[2] + o[3] * w5[3]);
;             lg6 += (o[0] * w6[0] + o[1] * w6[1]) + (o[2] * w6[2] + o[3] * w6[3]); lg7 += (o[0] * w7[0] + o[1] * w7[1]) + (o[2] * w7[2] + o[3] * w7[3]);
; #pragma unroll
;             for (int jj = 0; jj < 7; ++jj) v[jj] = v[jj + 1];
;         }
	v_mov_b32_e32 v126, v142
	v_mov_b32_e32 v127, v139
	v_pk_mov_b32 v[138:139], v[142:143], v[138:139] op_sel:[1,0]
	v_mov_b32_e32 v142, v144
	v_mov_b32_e32 v143, v141
	v_pk_mov_b32 v[140:141], v[144:145], v[140:141] op_sel:[1,0]
	s_waitcnt lgkmcnt(4)
	v_pk_mov_b32 v[144:145], v[146:147], v[150:151] op_sel:[1,0]
	v_mov_b32_e32 v147, v151
	v_pk_mov_b32 v[150:151], v[148:149], v[152:153] op_sel:[1,0]
	v_mov_b32_e32 v149, v153
	s_waitcnt lgkmcnt(2)
	v_pk_mov_b32 v[152:153], v[154:155], v[158:159] op_sel:[1,0]
	v_mov_b32_e32 v155, v159
	v_pk_mov_b32 v[158:159], v[156:157], v[160:161] op_sel:[1,0]
	v_mov_b32_e32 v157, v161
	s_waitcnt lgkmcnt(0)
	v_pk_mov_b32 v[160:161], v[162:163], v[166:167] op_sel:[1,0]
	v_mov_b32_e32 v163, v167
	v_pk_mov_b32 v[166:167], v[164:165], v[168:169] op_sel:[1,0]
	v_mov_b32_e32 v165, v169
	v_pk_mul_f32 v[126:127], v[118:119], v[126:127]
	v_pk_mul_f32 v[142:143], v[116:117], v[142:143]
	v_pk_mul_f32 v[146:147], v[118:119], v[146:147]
	v_pk_mul_f32 v[148:149], v[116:117], v[148:149]
	v_pk_mul_f32 v[154:155], v[118:119], v[154:155]
	v_pk_mul_f32 v[156:157], v[116:117], v[156:157]
	v_pk_mul_f32 v[162:163], v[118:119], v[162:163]
	v_pk_mul_f32 v[164:165], v[116:117], v[164:165]
	v_pk_fma_f32 v[126:127], v[118:119], v[138:139], v[126:127] op_sel:[1,0,0] op_sel_hi:[0,1,1]
	v_pk_fma_f32 v[138:139], v[116:117], v[140:141], v[142:143] op_sel:[1,0,0] op_sel_hi:[0,1,1]
	v_pk_fma_f32 v[140:141], v[118:119], v[144:145], v[146:147] op_sel:[1,0,0] op_sel_hi:[0,1,1]
	v_pk_fma_f32 v[142:143], v[116:117], v[150:151], v[148:149] op_sel:[1,0,0] op_sel_hi:[0,1,1]
	v_pk_fma_f32 v[144:145], v[118:119], v[152:153], v[154:155] op_sel:[1,0,0] op_sel_hi:[0,1,1]
	v_pk_fma_f32 v[146:147], v[116:117], v[158:159], v[156:157] op_sel:[1,0,0] op_sel_hi:[0,1,1]
	v_pk_fma_f32 v[148:149], v[118:119], v[160:161], v[162:163] op_sel:[1,0,0] op_sel_hi:[0,1,1]
	v_pk_fma_f32 v[150:151], v[116:117], v[166:167], v[164:165] op_sel:[1,0,0] op_sel_hi:[0,1,1]
	s_addk_i32 s7, 0x400
	s_add_i32 s6, s6, 32
	v_pk_add_f32 v[126:127], v[126:127], v[138:139]
	v_pk_add_f32 v[138:139], v[140:141], v[142:143]
	v_pk_add_f32 v[140:141], v[144:145], v[146:147]
	v_pk_add_f32 v[142:143], v[148:149], v[150:151]
	v_pk_add_f32 v[80:81], v[80:81], v[126:127]
	v_pk_add_f32 v[124:125], v[124:125], v[138:139]
	v_pk_add_f32 v[94:95], v[94:95], v[140:141]
	v_pk_add_f32 v[92:93], v[92:93], v[142:143]
	s_and_b32 s8, s7, 0x400
	s_and_b32 s9, s6, 0xc0
	s_lshl_b32 s8, s8, 2
	v_or_b32_e32 v126, s9, v128
	s_add_i32 s8, s8, 0
	v_lshl_add_u32 v126, v126, 4, s8
	ds_read_b128 v[138:141], v126
	ds_read_b128 v[142:145], v126 offset:8192
	ds_read_b128 v[146:149], v126 offset:16384
	ds_read_b128 v[150:153], v126 offset:24576
	ds_read_b128 v[154:157], v126 offset:32768
	ds_read_b128 v[158:161], v126 offset:40960
	ds_read_b128 v[162:165], v126 offset:49152
	ds_read_b128 v[166:169], v126 offset:57344
	s_waitcnt lgkmcnt(6)
	v_mov_b32_e32 v126, v142
	v_mov_b32_e32 v127, v139
	v_pk_mov_b32 v[138:139], v[142:143], v[138:139] op_sel:[1,0]
	v_mov_b32_e32 v142, v144
	v_mov_b32_e32 v143, v141
	v_pk_mov_b32 v[140:141], v[144:145], v[140:141] op_sel:[1,0]
	s_waitcnt lgkmcnt(4)
	v_pk_mov_b32 v[144:145], v[146:147], v[150:151] op_sel:[1,0]
	v_mov_b32_e32 v147, v151
	v_pk_mov_b32 v[150:151], v[148:149], v[152:153] op_sel:[1,0]
	v_mov_b32_e32 v149, v153
	s_waitcnt lgkmcnt(2)
	v_pk_mov_b32 v[152:153], v[154:155], v[158:159] op_sel:[1,0]
	v_mov_b32_e32 v155, v159
	v_pk_mov_b32 v[158:159], v[156:157], v[160:161] op_sel:[1,0]
	v_mov_b32_e32 v157, v161
	s_waitcnt lgkmcnt(0)
	v_pk_mov_b32 v[160:161], v[162:163], v[166:167] op_sel:[1,0]
	v_mov_b32_e32 v163, v167
	v_pk_mov_b32 v[166:167], v[164:165], v[168:169] op_sel:[1,0]
	v_mov_b32_e32 v165, v169
	v_pk_mul_f32 v[126:127], v[122:123], v[126:127]
	v_pk_mul_f32 v[142:143], v[120:121], v[142:143]
	v_pk_mul_f32 v[146:147], v[122:123], v[146:147]
	v_pk_mul_f32 v[148:149], v[120:121], v[148:149]
	v_pk_mul_f32 v[154:155], v[122:123], v[154:155]
	v_pk_mul_f32 v[156:157], v[120:121], v[156:157]
	v_pk_mul_f32 v[162:163], v[122:123], v[162:163]
	v_pk_mul_f32 v[164:165], v[120:121], v[164:165]
	v_pk_fma_f32 v[126:127], v[122:123], v[138:139], v[126:127] op_sel:[1,0,0] op_sel_hi:[0,1,1]
	v_pk_fma_f32 v[138:139], v[120:121], v[140:141], v[142:143] op_sel:[1,0,0] op_sel_hi:[0,1,1]
	v_pk_fma_f32 v[140:141], v[122:123], v[144:145], v[146:147] op_sel:[1,0,0] op_sel_hi:[0,1,1]
	v_pk_fma_f32 v[142:143], v[120:121], v[150:151], v[148:149] op_sel:[1,0,0] op_sel_hi:[0,1,1]
	v_pk_fma_f32 v[144:145], v[122:123], v[152:153], v[154:155] op_sel:[1,0,0] op_sel_hi:[0,1,1]
	v_pk_fma_f32 v[146:147], v[120:121], v[158:159], v[156:157] op_sel:[1,0,0] op_sel_hi:[0,1,1]
	v_pk_fma_f32 v[148:149], v[122:123], v[160:161], v[162:163] op_sel:[1,0,0] op_sel_hi:[0,1,1]
	v_pk_fma_f32 v[150:151], v[120:121], v[166:167], v[164:165] op_sel:[1,0,0] op_sel_hi:[0,1,1]
	s_addk_i32 s7, 0x400
	s_add_i32 s6, s6, 32
	v_pk_add_f32 v[126:127], v[126:127], v[138:139]
	v_pk_add_f32 v[138:139], v[140:141], v[142:143]
	v_pk_add_f32 v[140:141], v[144:145], v[146:147]
	v_pk_add_f32 v[142:143], v[148:149], v[150:151]
	v_pk_add_f32 v[80:81], v[80:81], v[126:127]
	v_pk_add_f32 v[124:125], v[124:125], v[138:139]
	v_pk_add_f32 v[94:95], v[94:95], v[140:141]
	v_pk_add_f32 v[92:93], v[92:93], v[142:143]
	s_and_b32 s8, s7, 0x400
	s_and_b32 s9, s6, 0xc0
	s_lshl_b32 s8, s8, 2
	v_or_b32_e32 v126, s9, v128
	s_add_i32 s8, s8, 0
	v_lshl_add_u32 v126, v126, 4, s8
	ds_read_b128 v[138:141], v126
	ds_read_b128 v[142:145], v126 offset:8192
	ds_read_b128 v[146:149], v126 offset:16384
	ds_read_b128 v[150:153], v126 offset:24576
	ds_read_b128 v[154:157], v126 offset:32768
	ds_read_b128 v[158:161], v126 offset:40960
	ds_read_b128 v[162:165], v126 offset:49152
	ds_read_b128 v[166:169], v126 offset:57344
	s_waitcnt lgkmcnt(6)
; #define LAS __attribute__((address_space(3)))
; template <bool ROUTE, bool COMBINE> ...
;     ...
;         for (int j = 0; j < 8; ++j) {
;             const f32x4 o = v[0]; const LAS float* wp = wT + (j & 1) * 1024 + ((j >> 1) * 64 + lane) * 4;
;             const f32x4 w0 = *(const LAS f32x4*)(wp), w1 = *(const LAS f32x4*)(wp + 2048), w2 = *(const LAS f32x4*)(wp + 2 * 2048), w3 = *(const LAS f32x4*)(wp + 3 * 2048);
;             const f32x4 w4 = *(const LAS f32x4*)(wp + 4 * 2048), w5 = *(const LAS f32x4*)(wp + 5 * 2048), w6 = *(const LAS f32x4*)(wp + 6 * 2048), w7 = *(const LAS f32x4*)(wp + 7 * 2048);
;             lg0 += (o[0] * w0[0] + o[1] * w0[1]) + (o[2] * w0[2] + o[3] * w0[3]); lg1 += (o[0] * w1[0] + o[1] * w1[1]) + (o[2] * w1[2] + o[3] * w1[3]);
;             lg2 += (o[0] * w2[0] + o[1] * w2[1]) + (o[2] * w2[2] + o[3] * w2[3]); lg3 += (o[0] * w3[0] + o[1] * w3[1]) + (o[2] * w3[2] + o[3] * w3[3]);
;             lg4 += (o[0] * w4[0] + o[1] * w4[1]) + (o[2] * w4[2] + o[3] * w4[3]); lg5 += (o[0] * w5[0] + o[1] * w5[1]) + (o[2] * w5[2] + o[3] * w5[3]);
;             lg6 += (o[0] * w6[0] + o[1] * w6[1]) + (o[2] * w6[2] + o[3] * w6[3]); lg7 += (o[0] * w7[0] + o[1] * w7[1]) + (o[2] * w7[2] + o[3] * w7[3]);
; #pragma unroll
;             for (int jj = 0; jj < 7; ++jj) v[jj] = v[jj + 1];
;         }
;         float lg[8] = {wave_sum(lg0), wave_sum(lg1), wave_sum(lg2), wave_sum(lg3), wave_sum(lg4), wave_sum(lg5), wave_sum(lg6), wave_sum(lg7)};
	v_mov_b32_e32 v126, v142
	v_mov_b32_e32 v127, v139
	v_pk_mov_b32 v[138:139], v[142:143], v[138:139] op_sel:[1,0]
	v_mov_b32_e32 v142, v144
	v_mov_b32_e32 v143, v141
	v_pk_mov_b32 v[140:141], v[144:145], v[140:141] op_sel:[1,0]
	s_waitcnt lgkmcnt(4)
	v_pk_mov_b32 v[144:145], v[146:147], v[150:151] op_sel:[1,0]
	v_mov_b32_e32 v147, v151
	v_pk_mov_b32 v[150:151], v[148:149], v[152:153] op_sel:[1,0]
	v_mov_b32_e32 v149, v153
	s_waitcnt lgkmcnt(2)
	v_pk_mov_b32 v[152:153], v[154:155], v[158:159] op_sel:[1,0]
	v_mov_b32_e32 v155, v159
	v_pk_mov_b32 v[158:159], v[156:157], v[160:161] op_sel:[1,0]
	v_mov_b32_e32 v157, v161
	s_waitcnt lgkmcnt(0)
	v_pk_mov_b32 v[160:161], v[162:163], v[166:167] op_sel:[1,0]
	v_mov_b32_e32 v163, v167
	v_pk_mov_b32 v[166:167], v[164:165], v[168:169] op_sel:[1,0]
	v_mov_b32_e32 v165, v169
	v_pk_mul_f32 v[126:127], v[108:109], v[126:127]
	v_pk_mul_f32 v[142:143], v[106:107], v[142:143]
	v_pk_mul_f32 v[146:147], v[108:109], v[146:147]
	v_pk_mul_f32 v[148:149], v[106:107], v[148:149]
	v_pk_mul_f32 v[154:155], v[108:109], v[154:155]
	v_pk_mul_f32 v[156:157], v[106:107], v[156:157]
	v_pk_mul_f32 v[162:163], v[108:109], v[162:163]
	v_pk_mul_f32 v[164:165], v[106:107], v[164:165]
	v_pk_fma_f32 v[126:127], v[108:109], v[138:139], v[126:127] op_sel:[1,0,0] op_sel_hi:[0,1,1]
	v_pk_fma_f32 v[138:139], v[106:107], v[140:141], v[142:143] op_sel:[1,0,0] op_sel_hi:[0,1,1]
	v_pk_fma_f32 v[140:141], v[108:109], v[144:145], v[146:147] op_sel:[1,0,0] op_sel_hi:[0,1,1]
	v_pk_fma_f32 v[142:143], v[106:107], v[150:151], v[148:149] op_sel:[1,0,0] op_sel_hi:[0,1,1]
	v_pk_fma_f32 v[144:145], v[108:109], v[152:153], v[154:155] op_sel:[1,0,0] op_sel_hi:[0,1,1]
	v_pk_fma_f32 v[146:147], v[106:107], v[158:159], v[156:157] op_sel:[1,0,0] op_sel_hi:[0,1,1]
	v_pk_fma_f32 v[148:149], v[108:109], v[160:161], v[162:163] op_sel:[1,0,0] op_sel_hi:[0,1,1]
	v_pk_fma_f32 v[150:151], v[106:107], v[166:167], v[164:165] op_sel:[1,0,0] op_sel_hi:[0,1,1]
	s_addk_i32 s7, 0x400
	s_add_i32 s6, s6, 32
	v_pk_add_f32 v[126:127], v[126:127], v[138:139]
	v_pk_add_f32 v[138:139], v[140:141], v[142:143]
	v_pk_add_f32 v[140:141], v[144:145], v[146:147]
	v_pk_add_f32 v[142:143], v[148:149], v[150:151]
	v_pk_add_f32 v[80:81], v[80:81], v[126:127]
	v_pk_add_f32 v[124:125], v[124:125], v[138:139]
	v_pk_add_f32 v[94:95], v[94:95], v[140:141]
	v_pk_add_f32 v[92:93], v[92:93], v[142:143]
	s_and_b32 s8, s7, 0x400
	s_and_b32 s9, s6, 0xc0
	s_lshl_b32 s8, s8, 2
	v_or_b32_e32 v126, s9, v128
	s_add_i32 s8, s8, 0
	v_lshl_add_u32 v126, v126, 4, s8
	ds_read_b128 v[138:141], v126
	ds_read_b128 v[142:145], v126 offset:8192
	ds_read_b128 v[146:149], v126 offset:16384
	ds_read_b128 v[150:153], v126 offset:24576
	ds_read_b128 v[154:157], v126 offset:32768
	ds_read_b128 v[158:161], v126 offset:40960
	ds_read_b128 v[162:165], v126 offset:49152
	ds_read_b128 v[166:169], v126 offset:57344
	s_waitcnt lgkmcnt(6)
	v_mov_b32_e32 v126, v142
	v_mov_b32_e32 v127, v139
	v_pk_mov_b32 v[138:139], v[142:143], v[138:139] op_sel:[1,0]
	v_mov_b32_e32 v142, v144
	v_mov_b32_e32 v143, v141
	v_pk_mov_b32 v[140:141], v[144:145], v[140:141] op_sel:[1,0]
	s_waitcnt lgkmcnt(4)
	v_pk_mov_b32 v[144:145], v[146:147], v[150:151] op_sel:[1,0]
	v_mov_b32_e32 v147, v151
	v_pk_mov_b32 v[150:151], v[148:149], v[152:153] op_sel:[1,0]
	v_mov_b32_e32 v149, v153
	s_waitcnt lgkmcnt(2)
	v_pk_mov_b32 v[152:153], v[154:155], v[158:159] op_sel:[1,0]
	v_mov_b32_e32 v155, v159
	v_pk_mov_b32 v[158:159], v[156:157], v[160:161] op_sel:[1,0]
	v_mov_b32_e32 v157, v161
	s_waitcnt lgkmcnt(0)
	v_pk_mov_b32 v[160:161], v[162:163], v[166:167] op_sel:[1,0]
	v_mov_b32_e32 v163, v167
	v_pk_mov_b32 v[166:167], v[164:165], v[168:169] op_sel:[1,0]
	v_mov_b32_e32 v165, v169
	v_pk_mul_f32 v[126:127], v[104:105], v[126:127]
	v_pk_mul_f32 v[142:143], v[102:103], v[142:143]
	v_pk_mul_f32 v[146:147], v[104:105], v[146:147]
	v_pk_mul_f32 v[148:149], v[102:103], v[148:149]
	v_pk_mul_f32 v[154:155], v[104:105], v[154:155]
	v_pk_mul_f32 v[156:157], v[102:103], v[156:157]
	v_pk_mul_f32 v[162:163], v[104:105], v[162:163]
	v_pk_mul_f32 v[164:165], v[102:103], v[164:165]
	v_pk_fma_f32 v[126:127], v[104:105], v[138:139], v[126:127] op_sel:[1,0,0] op_sel_hi:[0,1,1]
	v_pk_fma_f32 v[138:139], v[102:103], v[140:141], v[142:143] op_sel:[1,0,0] op_sel_hi:[0,1,1]
	v_pk_fma_f32 v[140:141], v[104:105], v[144:145], v[146:147] op_sel:[1,0,0] op_sel_hi:[0,1,1]
	v_pk_fma_f32 v[142:143], v[102:103], v[150:151], v[148:149] op_sel:[1,0,0] op_sel_hi:[0,1,1]
	v_pk_fma_f32 v[144:145], v[104:105], v[152:153], v[154:155] op_sel:[1,0,0] op_sel_hi:[0,1,1]
	v_pk_fma_f32 v[146:147], v[102:103], v[158:159], v[156:157] op_sel:[1,0,0] op_sel_hi:[0,1,1]
	v_pk_fma_f32 v[148:149], v[104:105], v[160:161], v[162:163] op_sel:[1,0,0] op_sel_hi:[0,1,1]
	v_pk_fma_f32 v[150:151], v[102:103], v[166:167], v[164:165] op_sel:[1,0,0] op_sel_hi:[0,1,1]
	s_addk_i32 s7, 0x400
	s_add_i32 s6, s6, 32
	v_pk_add_f32 v[126:127], v[126:127], v[138:139]
	v_pk_add_f32 v[138:139], v[140:141], v[142:143]
	v_pk_add_f32 v[140:141], v[144:145], v[146:147]
	v_pk_add_f32 v[142:143], v[148:149], v[150:151]
	v_pk_add_f32 v[80:81], v[80:81], v[126:127]
	v_pk_add_f32 v[124:125], v[124:125], v[138:139]
	v_pk_add_f32 v[94:95], v[94:95], v[140:141]
	v_pk_add_f32 v[92:93], v[92:93], v[142:143]
	ds_bpermute_b32 v83, v129, v81
	ds_bpermute_b32 v82, v129, v80
	ds_bpermute_b32 v84, v129, v124
	ds_bpermute_b32 v85, v129, v125
	ds_bpermute_b32 v86, v129, v94
	ds_bpermute_b32 v91, v129, v95
	s_waitcnt lgkmcnt(4)
	v_pk_add_f32 v[80:81], v[80:81], v[82:83]
	ds_bpermute_b32 v83, v130, v81
	ds_bpermute_b32 v82, v130, v80
	s_waitcnt lgkmcnt(5)
; template <bool ROUTE, bool COMBINE> ...
;     ...
;         float lg[8] = {wave_sum(lg0), wave_sum(lg1), wave_sum(lg2), wave_sum(lg3), wave_sum(lg4), wave_sum(lg5), wave_sum(lg6), wave_sum(lg7)};
;         if (lane == 0) {
;             int i0 = 0; float v0 = lg[0];
; #pragma unroll
;             for (int e = 1; e < 8; ++e) if (lg[e] > v0) { v0 = lg[e]; i0 = e; }
;             int i1 = -1; float v1 = -3.0e38f;
; #pragma unroll
;             for (int e = 0; e < 8; ++e) if (e != i0 && lg[e] > v1) { v1 = lg[e]; i1 = e; }
;             const float e1 = expf(v1 - v0), g0 = 1.0f / (1.0f + e1), g1 = e1 / (1.0f + e1);
;             tope[row * 2] = i0; tope[row * 2 + 1] = i1; topg[row * 2] = g0; topg[row * 2 + 1] = g1;
	v_add_f32_e32 v84, v124, v84
	ds_bpermute_b32 v87, v130, v84
	s_waitcnt lgkmcnt(5)
	v_add_f32_e32 v85, v125, v85
	s_waitcnt lgkmcnt(4)
	v_add_f32_e32 v86, v94, v86
	s_waitcnt lgkmcnt(1)
	v_pk_add_f32 v[80:81], v[80:81], v[82:83]
	ds_bpermute_b32 v83, v131, v81
	ds_bpermute_b32 v82, v131, v80
	s_waitcnt lgkmcnt(2)
	v_add_f32_e32 v84, v84, v87
	ds_bpermute_b32 v88, v130, v85
	ds_bpermute_b32 v89, v130, v86
	ds_bpermute_b32 v87, v131, v84
	s_waitcnt lgkmcnt(3)
	v_pk_add_f32 v[80:81], v[80:81], v[82:83]
	ds_bpermute_b32 v83, v132, v81
	ds_bpermute_b32 v82, v132, v80
	s_waitcnt lgkmcnt(4)
	v_add_f32_e32 v85, v85, v88
	s_waitcnt lgkmcnt(2)
	v_add_f32_e32 v84, v84, v87
	ds_bpermute_b32 v88, v131, v85
	ds_bpermute_b32 v87, v132, v84
	s_waitcnt lgkmcnt(2)
	v_pk_add_f32 v[80:81], v[80:81], v[82:83]
	ds_bpermute_b32 v83, v133, v81
	ds_bpermute_b32 v82, v133, v80
	s_waitcnt lgkmcnt(3)
	v_add_f32_e32 v85, v85, v88
	s_waitcnt lgkmcnt(2)
	v_add_f32_e32 v84, v84, v87
	ds_bpermute_b32 v87, v132, v85
	ds_bpermute_b32 v88, v133, v84
	s_waitcnt lgkmcnt(2)
	v_pk_add_f32 v[80:81], v[80:81], v[82:83]
	v_add_f32_e32 v82, v86, v89
	ds_bpermute_b32 v86, v131, v82
	s_waitcnt lgkmcnt(2)
	v_add_f32_e32 v87, v85, v87
	s_waitcnt lgkmcnt(1)
	v_add_f32_e32 v85, v84, v88
	ds_bpermute_b32 v94, v129, v93
	v_add_f32_e32 v91, v95, v91
	s_waitcnt lgkmcnt(1)
	v_add_f32_e32 v86, v82, v86
	ds_bpermute_b32 v89, v132, v86
	ds_bpermute_b32 v95, v130, v91
	s_waitcnt lgkmcnt(2)
	v_add_f32_e32 v93, v93, v94
	ds_bpermute_b32 v94, v130, v93
	ds_bpermute_b32 v90, v133, v87
	s_waitcnt lgkmcnt(3)
	v_add_f32_e32 v84, v86, v89
	ds_bpermute_b32 v89, v133, v84
	s_waitcnt lgkmcnt(3)
	v_add_f32_e32 v91, v91, v95
	s_waitcnt lgkmcnt(2)
	v_add_f32_e32 v93, v93, v94
	ds_bpermute_b32 v95, v131, v91
	ds_bpermute_b32 v94, v131, v93
	s_waitcnt lgkmcnt(2)
	v_add_f32_e32 v89, v84, v89
	ds_bpermute_b32 v84, v129, v92
	v_add_f32_e32 v87, v87, v90
	s_waitcnt lgkmcnt(2)
	v_add_f32_e32 v91, v91, v95
	s_waitcnt lgkmcnt(1)
	v_add_f32_e32 v93, v93, v94
	ds_bpermute_b32 v95, v132, v91
	s_waitcnt lgkmcnt(1)
	v_add_f32_e32 v84, v92, v84
	ds_bpermute_b32 v92, v130, v84
	ds_bpermute_b32 v94, v132, v93
	ds_bpermute_b32 v83, v134, v81
	s_waitcnt lgkmcnt(3)
	v_add_f32_e32 v91, v91, v95
	ds_bpermute_b32 v95, v133, v91
	s_waitcnt lgkmcnt(3)
	v_add_f32_e32 v84, v84, v92
	ds_bpermute_b32 v92, v131, v84
	s_waitcnt lgkmcnt(3)
	v_add_f32_e32 v103, v93, v94
	ds_bpermute_b32 v104, v133, v103
	s_waitcnt lgkmcnt(2)
	v_add_f32_e32 v91, v91, v95
	ds_bpermute_b32 v82, v134, v80
	s_waitcnt lgkmcnt(2)
	v_add_f32_e32 v84, v84, v92
	ds_bpermute_b32 v92, v132, v84
	ds_bpermute_b32 v86, v134, v85
	ds_bpermute_b32 v88, v134, v87
	ds_bpermute_b32 v90, v134, v89
	s_waitcnt lgkmcnt(3)
	v_add_f32_e32 v84, v84, v92
	ds_bpermute_b32 v102, v133, v84
	ds_bpermute_b32 v92, v134, v91
	s_waitcnt lgkmcnt(1)
	v_add_f32_e32 v93, v84, v102
	v_add_f32_e32 v84, v103, v104
	ds_bpermute_b32 v94, v134, v93
	ds_bpermute_b32 v95, v134, v84
	s_and_saveexec_b64 s[22:23], s[4:5]
	s_cbranch_execz .LBB0_1374
	v_add_f32_e32 v88, v87, v88
	v_add_f32_e32 v85, v85, v86
	v_pk_add_f32 v[86:87], v[80:81], v[82:83]
	v_add_f32_e32 v89, v89, v90
	v_cmp_gt_f32_e32 vcc, v86, v87
	s_waitcnt lgkmcnt(2)
	v_add_f32_e32 v91, v91, v92
	s_waitcnt lgkmcnt(1)
	v_add_f32_e32 v93, v93, v94
	v_cndmask_b32_e32 v81, v87, v86, vcc
	v_cndmask_b32_e64 v80, 0, 1, vcc
	v_cmp_gt_f32_e32 vcc, v85, v81
	s_waitcnt lgkmcnt(0)
	v_add_f32_e32 v84, v84, v95
	v_cmp_nlt_f32_e64 s[12:13], s35, v87
	v_cndmask_b32_e32 v81, v81, v85, vcc
	v_cndmask_b32_e64 v80, v80, 2, vcc
	v_cmp_gt_f32_e32 vcc, v88, v81
	s_nop 1
	v_cndmask_b32_e32 v81, v81, v88, vcc
	v_cndmask_b32_e64 v80, v80, 3, vcc
	v_cmp_gt_f32_e32 vcc, v89, v81
	s_nop 1
	v_cndmask_b32_e32 v81, v81, v89, vcc
	v_cndmask_b32_e64 v80, v80, 4, vcc
	v_cmp_gt_f32_e32 vcc, v91, v81
	s_nop 1
	v_cndmask_b32_e32 v81, v81, v91, vcc
	v_cndmask_b32_e64 v80, v80, 5, vcc
	v_cmp_ngt_f32_e32 vcc, v93, v81
	s_nop 1
	v_cndmask_b32_e32 v82, v93, v81, vcc
	v_cndmask_b32_e32 v80, 6, v80, vcc
	v_cmp_gt_f32_e64 s[8:9], v84, v82
	v_cmp_ngt_f32_e64 s[6:7], v84, v82
	s_nop 0
	v_cndmask_b32_e64 v80, v80, 7, s[8:9]
	v_cmp_eq_u32_e64 s[10:11], 0, v80
	s_or_b64 s[10:11], s[10:11], s[12:13]
	s_or_b64 s[8:9], vcc, s[8:9]
	v_cndmask_b32_e64 v83, v87, v136, s[10:11]
	v_cndmask_b32_e64 v81, 0, -1, s[10:11]
	v_cmp_ne_u32_e64 s[10:11], 1, v80
	v_cmp_gt_f32_e64 s[12:13], v86, v83
	s_and_b64 s[10:11], s[10:11], s[12:13]
	v_cndmask_b32_e64 v83, v83, v86, s[10:11]
	v_cndmask_b32_e64 v81, v81, 1, s[10:11]
	v_cmp_ne_u32_e64 s[10:11], 2, v80
	v_cmp_gt_f32_e64 s[12:13], v85, v83
	s_and_b64 s[10:11], s[10:11], s[12:13]
	v_cndmask_b32_e64 v83, v83, v85, s[10:11]
	v_cndmask_b32_e64 v81, v81, 2, s[10:11]
	v_cmp_ne_u32_e64 s[10:11], 3, v80
	v_cmp_gt_f32_e64 s[12:13], v88, v83
	s_and_b64 s[10:11], s[10:11], s[12:13]
	v_cndmask_b32_e64 v83, v83, v88, s[10:11]
	v_cndmask_b32_e64 v81, v81, 3, s[10:11]
	v_cmp_ne_u32_e64 s[10:11], 4, v80
	v_cmp_gt_f32_e64 s[12:13], v89, v83
	s_and_b64 s[10:11], s[10:11], s[12:13]
	v_cndmask_b32_e64 v83, v83, v89, s[10:11]
	v_cndmask_b32_e64 v81, v81, 4, s[10:11]
	v_cmp_ne_u32_e64 s[10:11], 5, v80
	v_cmp_gt_f32_e64 s[12:13], v91, v83
	s_and_b64 s[10:11], s[10:11], s[12:13]
	v_cndmask_b32_e64 v83, v83, v91, s[10:11]
	v_cmp_gt_f32_e32 vcc, v93, v83
	v_cndmask_b32_e64 v81, v81, 5, s[10:11]
	s_and_b64 vcc, s[8:9], vcc
	v_cndmask_b32_e64 v81, v81, 6, vcc
	v_cndmask_b32_e32 v83, v83, v93, vcc
	s_and_saveexec_b64 s[8:9], s[6:7]
	s_cbranch_execz .LBB0_1373
	v_cmp_gt_f32_e32 vcc, v84, v83
	s_and_saveexec_b64 s[6:7], vcc
	s_cbranch_execz .LBB0_1372
	v_mov_b32_e32 v81, 7
	v_mov_b32_e32 v83, v84
	s_branch .LBB0_1372
